# v52 + merge-gate sigmoid-to-u8 epilogue path rewritten with fewer VALU ops (packed mul/add, fma-clamp, +2^23 rounding, v_perm byte gather); f32 math unchanged in kind
# speedup vs baseline: 1.0068x; 1.0068x over previous
.LBB0_3473:
	s_mov_b32 s4, 0xbfb8aa3b
	s_mov_b32 s6, 0x4b000000
	s_mov_b32 s54, 0x3b808081
	s_mov_b32 s55, 0x0c0c0400
	v_lshl_add_u32 v66, s51, 8, v251
	v_mov_b32_e32 v67, v1
	v_lshl_add_u64 v[66:67], s[46:47], 0, v[66:67]
	v_pk_mul_f32 v[190:191], v[190:191], s[4:5] op_sel_hi:[1,0]
	v_pk_mul_f32 v[192:193], v[192:193], s[4:5] op_sel_hi:[1,0]
	v_exp_f32_e32 v190, v190
	v_exp_f32_e32 v191, v191
	v_exp_f32_e32 v192, v192
	v_exp_f32_e32 v193, v193
	v_fma_f32 v190, v190, s54, s54 clamp
	v_fma_f32 v191, v191, s54, s54 clamp
	v_fma_f32 v192, v192, s54, s54 clamp
	v_fma_f32 v193, v193, s54, s54 clamp
	v_rcp_f32_e32 v190, v190
	v_rcp_f32_e32 v191, v191
	v_rcp_f32_e32 v192, v192
	v_rcp_f32_e32 v193, v193
	v_mad_i64_i32 v[80:81], vcc, v18, s64, v[66:67]
	v_pk_add_f32 v[190:191], v[190:191], s[6:7] op_sel_hi:[1,0]
	v_pk_add_f32 v[192:193], v[192:193], s[6:7] op_sel_hi:[1,0]
	v_perm_b32 v68, v191, v190, s55
	v_perm_b32 v69, v193, v192, s55
	v_lshl_or_b32 v70, v69, 16, v68
	v_pk_mul_f32 v[186:187], v[186:187], s[4:5] op_sel_hi:[1,0]
	v_pk_mul_f32 v[188:189], v[188:189], s[4:5] op_sel_hi:[1,0]
	v_exp_f32_e32 v186, v186
	v_exp_f32_e32 v187, v187
	v_exp_f32_e32 v188, v188
	v_exp_f32_e32 v189, v189
	v_fma_f32 v186, v186, s54, s54 clamp
	v_fma_f32 v187, v187, s54, s54 clamp
	v_fma_f32 v188, v188, s54, s54 clamp
	v_fma_f32 v189, v189, s54, s54 clamp
	v_rcp_f32_e32 v186, v186
	v_rcp_f32_e32 v187, v187
	v_rcp_f32_e32 v188, v188
	v_rcp_f32_e32 v189, v189
	v_pk_add_f32 v[186:187], v[186:187], s[6:7] op_sel_hi:[1,0]
	v_pk_add_f32 v[188:189], v[188:189], s[6:7] op_sel_hi:[1,0]
	v_perm_b32 v68, v187, v186, s55
	v_perm_b32 v69, v189, v188, s55
	v_lshl_or_b32 v71, v69, 16, v68
	v_pk_mul_f32 v[158:159], v[158:159], s[4:5] op_sel_hi:[1,0]
	v_pk_mul_f32 v[160:161], v[160:161], s[4:5] op_sel_hi:[1,0]
	v_exp_f32_e32 v158, v158
	v_exp_f32_e32 v159, v159
	v_exp_f32_e32 v160, v160
	v_exp_f32_e32 v161, v161
	v_fma_f32 v158, v158, s54, s54 clamp
	v_fma_f32 v159, v159, s54, s54 clamp
	v_fma_f32 v160, v160, s54, s54 clamp
	v_fma_f32 v161, v161, s54, s54 clamp
	v_rcp_f32_e32 v158, v158
	v_rcp_f32_e32 v159, v159
	v_rcp_f32_e32 v160, v160
	v_rcp_f32_e32 v161, v161
	v_pk_add_f32 v[158:159], v[158:159], s[6:7] op_sel_hi:[1,0]
	v_pk_add_f32 v[160:161], v[160:161], s[6:7] op_sel_hi:[1,0]
	v_perm_b32 v68, v159, v158, s55
	v_perm_b32 v69, v161, v160, s55
	v_lshl_or_b32 v72, v69, 16, v68
	v_pk_mul_f32 v[154:155], v[154:155], s[4:5] op_sel_hi:[1,0]
	v_pk_mul_f32 v[156:157], v[156:157], s[4:5] op_sel_hi:[1,0]
	v_exp_f32_e32 v154, v154
	v_exp_f32_e32 v155, v155
	v_exp_f32_e32 v156, v156
	v_exp_f32_e32 v157, v157
	v_fma_f32 v154, v154, s54, s54 clamp
	v_fma_f32 v155, v155, s54, s54 clamp
	v_fma_f32 v156, v156, s54, s54 clamp
	v_fma_f32 v157, v157, s54, s54 clamp
	v_rcp_f32_e32 v154, v154
	v_rcp_f32_e32 v155, v155
	v_rcp_f32_e32 v156, v156
	v_rcp_f32_e32 v157, v157
	v_pk_add_f32 v[154:155], v[154:155], s[6:7] op_sel_hi:[1,0]
	v_pk_add_f32 v[156:157], v[156:157], s[6:7] op_sel_hi:[1,0]
	v_perm_b32 v68, v155, v154, s55
	v_perm_b32 v69, v157, v156, s55
	v_lshl_or_b32 v73, v69, 16, v68
	global_store_dwordx4 v[80:81], v[70:73], off
	v_add_u32_e32 v78, 0x10, v18
	v_pk_mul_f32 v[182:183], v[182:183], s[4:5] op_sel_hi:[1,0]
	v_pk_mul_f32 v[184:185], v[184:185], s[4:5] op_sel_hi:[1,0]
	v_exp_f32_e32 v182, v182
	v_exp_f32_e32 v183, v183
	v_exp_f32_e32 v184, v184
	v_exp_f32_e32 v185, v185
	v_fma_f32 v182, v182, s54, s54 clamp
	v_fma_f32 v183, v183, s54, s54 clamp
	v_fma_f32 v184, v184, s54, s54 clamp
	v_fma_f32 v185, v185, s54, s54 clamp
	v_rcp_f32_e32 v182, v182
	v_rcp_f32_e32 v183, v183
	v_rcp_f32_e32 v184, v184
	v_rcp_f32_e32 v185, v185
	v_mad_i64_i32 v[82:83], vcc, v78, s64, v[66:67]
	v_pk_add_f32 v[182:183], v[182:183], s[6:7] op_sel_hi:[1,0]
	v_pk_add_f32 v[184:185], v[184:185], s[6:7] op_sel_hi:[1,0]
	v_perm_b32 v68, v183, v182, s55
	v_perm_b32 v69, v185, v184, s55
	v_lshl_or_b32 v74, v69, 16, v68
	v_pk_mul_f32 v[178:179], v[178:179], s[4:5] op_sel_hi:[1,0]
	v_pk_mul_f32 v[180:181], v[180:181], s[4:5] op_sel_hi:[1,0]
	v_exp_f32_e32 v178, v178
	v_exp_f32_e32 v179, v179
	v_exp_f32_e32 v180, v180
	v_exp_f32_e32 v181, v181
	v_fma_f32 v178, v178, s54, s54 clamp
	v_fma_f32 v179, v179, s54, s54 clamp
	v_fma_f32 v180, v180, s54, s54 clamp
	v_fma_f32 v181, v181, s54, s54 clamp
	v_rcp_f32_e32 v178, v178
	v_rcp_f32_e32 v179, v179
	v_rcp_f32_e32 v180, v180
	v_rcp_f32_e32 v181, v181
	v_pk_add_f32 v[178:179], v[178:179], s[6:7] op_sel_hi:[1,0]
	v_pk_add_f32 v[180:181], v[180:181], s[6:7] op_sel_hi:[1,0]
	v_perm_b32 v68, v179, v178, s55
	v_perm_b32 v69, v181, v180, s55
	v_lshl_or_b32 v75, v69, 16, v68
	v_pk_mul_f32 v[150:151], v[150:151], s[4:5] op_sel_hi:[1,0]
	v_pk_mul_f32 v[152:153], v[152:153], s[4:5] op_sel_hi:[1,0]
	v_exp_f32_e32 v150, v150
	v_exp_f32_e32 v151, v151
	v_exp_f32_e32 v152, v152
	v_exp_f32_e32 v153, v153
	v_fma_f32 v150, v150, s54, s54 clamp
	v_fma_f32 v151, v151, s54, s54 clamp
	v_fma_f32 v152, v152, s54, s54 clamp
	v_fma_f32 v153, v153, s54, s54 clamp
	v_rcp_f32_e32 v150, v150
	v_rcp_f32_e32 v151, v151
	v_rcp_f32_e32 v152, v152
	v_rcp_f32_e32 v153, v153
	v_pk_add_f32 v[150:151], v[150:151], s[6:7] op_sel_hi:[1,0]
	v_pk_add_f32 v[152:153], v[152:153], s[6:7] op_sel_hi:[1,0]
	v_perm_b32 v68, v151, v150, s55
	v_perm_b32 v69, v153, v152, s55
	v_lshl_or_b32 v76, v69, 16, v68
	v_pk_mul_f32 v[146:147], v[146:147], s[4:5] op_sel_hi:[1,0]
	v_pk_mul_f32 v[148:149], v[148:149], s[4:5] op_sel_hi:[1,0]
	v_exp_f32_e32 v146, v146
	v_exp_f32_e32 v147, v147
	v_exp_f32_e32 v148, v148
	v_exp_f32_e32 v149, v149
	v_fma_f32 v146, v146, s54, s54 clamp
	v_fma_f32 v147, v147, s54, s54 clamp
	v_fma_f32 v148, v148, s54, s54 clamp
	v_fma_f32 v149, v149, s54, s54 clamp
	v_rcp_f32_e32 v146, v146
	v_rcp_f32_e32 v147, v147
	v_rcp_f32_e32 v148, v148
	v_rcp_f32_e32 v149, v149
	v_pk_add_f32 v[146:147], v[146:147], s[6:7] op_sel_hi:[1,0]
	v_pk_add_f32 v[148:149], v[148:149], s[6:7] op_sel_hi:[1,0]
	v_perm_b32 v68, v147, v146, s55
	v_perm_b32 v69, v149, v148, s55
	v_lshl_or_b32 v77, v69, 16, v68
	global_store_dwordx4 v[82:83], v[74:77], off
	v_add_u32_e32 v78, 0x20, v18
	v_pk_mul_f32 v[174:175], v[174:175], s[4:5] op_sel_hi:[1,0]
	v_pk_mul_f32 v[176:177], v[176:177], s[4:5] op_sel_hi:[1,0]
	v_exp_f32_e32 v174, v174
	v_exp_f32_e32 v175, v175
	v_exp_f32_e32 v176, v176
	v_exp_f32_e32 v177, v177
	v_fma_f32 v174, v174, s54, s54 clamp
	v_fma_f32 v175, v175, s54, s54 clamp
	v_fma_f32 v176, v176, s54, s54 clamp
	v_fma_f32 v177, v177, s54, s54 clamp
	v_rcp_f32_e32 v174, v174
	v_rcp_f32_e32 v175, v175
	v_rcp_f32_e32 v176, v176
	v_rcp_f32_e32 v177, v177
	v_mad_i64_i32 v[80:81], vcc, v78, s64, v[66:67]
	v_pk_add_f32 v[174:175], v[174:175], s[6:7] op_sel_hi:[1,0]
	v_pk_add_f32 v[176:177], v[176:177], s[6:7] op_sel_hi:[1,0]
	v_perm_b32 v68, v175, v174, s55
	v_perm_b32 v69, v177, v176, s55
	v_lshl_or_b32 v70, v69, 16, v68
	v_pk_mul_f32 v[170:171], v[170:171], s[4:5] op_sel_hi:[1,0]
	v_pk_mul_f32 v[172:173], v[172:173], s[4:5] op_sel_hi:[1,0]
	v_exp_f32_e32 v170, v170
	v_exp_f32_e32 v171, v171
	v_exp_f32_e32 v172, v172
	v_exp_f32_e32 v173, v173
	v_fma_f32 v170, v170, s54, s54 clamp
	v_fma_f32 v171, v171, s54, s54 clamp
	v_fma_f32 v172, v172, s54, s54 clamp
	v_fma_f32 v173, v173, s54, s54 clamp
	v_rcp_f32_e32 v170, v170
	v_rcp_f32_e32 v171, v171
	v_rcp_f32_e32 v172, v172
	v_rcp_f32_e32 v173, v173
	v_pk_add_f32 v[170:171], v[170:171], s[6:7] op_sel_hi:[1,0]
	v_pk_add_f32 v[172:173], v[172:173], s[6:7] op_sel_hi:[1,0]
	v_perm_b32 v68, v171, v170, s55
	v_perm_b32 v69, v173, v172, s55
	v_lshl_or_b32 v71, v69, 16, v68
	v_pk_mul_f32 v[142:143], v[142:143], s[4:5] op_sel_hi:[1,0]
	v_pk_mul_f32 v[144:145], v[144:145], s[4:5] op_sel_hi:[1,0]
	v_exp_f32_e32 v142, v142
	v_exp_f32_e32 v143, v143
	v_exp_f32_e32 v144, v144
	v_exp_f32_e32 v145, v145
	v_fma_f32 v142, v142, s54, s54 clamp
	v_fma_f32 v143, v143, s54, s54 clamp
	v_fma_f32 v144, v144, s54, s54 clamp
	v_fma_f32 v145, v145, s54, s54 clamp
	v_rcp_f32_e32 v142, v142
	v_rcp_f32_e32 v143, v143
	v_rcp_f32_e32 v144, v144
	v_rcp_f32_e32 v145, v145
	v_pk_add_f32 v[142:143], v[142:143], s[6:7] op_sel_hi:[1,0]
	v_pk_add_f32 v[144:145], v[144:145], s[6:7] op_sel_hi:[1,0]
	v_perm_b32 v68, v143, v142, s55
	v_perm_b32 v69, v145, v144, s55
	v_lshl_or_b32 v72, v69, 16, v68
	v_pk_mul_f32 v[138:139], v[138:139], s[4:5] op_sel_hi:[1,0]
	v_pk_mul_f32 v[140:141], v[140:141], s[4:5] op_sel_hi:[1,0]
	v_exp_f32_e32 v138, v138
	v_exp_f32_e32 v139, v139
	v_exp_f32_e32 v140, v140
	v_exp_f32_e32 v141, v141
	v_fma_f32 v138, v138, s54, s54 clamp
	v_fma_f32 v139, v139, s54, s54 clamp
	v_fma_f32 v140, v140, s54, s54 clamp
	v_fma_f32 v141, v141, s54, s54 clamp
	v_rcp_f32_e32 v138, v138
	v_rcp_f32_e32 v139, v139
	v_rcp_f32_e32 v140, v140
	v_rcp_f32_e32 v141, v141
	v_pk_add_f32 v[138:139], v[138:139], s[6:7] op_sel_hi:[1,0]
	v_pk_add_f32 v[140:141], v[140:141], s[6:7] op_sel_hi:[1,0]
	v_perm_b32 v68, v139, v138, s55
	v_perm_b32 v69, v141, v140, s55
	v_lshl_or_b32 v73, v69, 16, v68
	global_store_dwordx4 v[80:81], v[70:73], off
	v_add_u32_e32 v78, 0x30, v18
	v_pk_mul_f32 v[166:167], v[166:167], s[4:5] op_sel_hi:[1,0]
	v_pk_mul_f32 v[168:169], v[168:169], s[4:5] op_sel_hi:[1,0]
	v_exp_f32_e32 v166, v166
	v_exp_f32_e32 v167, v167
	v_exp_f32_e32 v168, v168
	v_exp_f32_e32 v169, v169
	v_fma_f32 v166, v166, s54, s54 clamp
	v_fma_f32 v167, v167, s54, s54 clamp
	v_fma_f32 v168, v168, s54, s54 clamp
	v_fma_f32 v169, v169, s54, s54 clamp
	v_rcp_f32_e32 v166, v166
	v_rcp_f32_e32 v167, v167
	v_rcp_f32_e32 v168, v168
	v_rcp_f32_e32 v169, v169
	v_mad_i64_i32 v[82:83], vcc, v78, s64, v[66:67]
	v_pk_add_f32 v[166:167], v[166:167], s[6:7] op_sel_hi:[1,0]
	v_pk_add_f32 v[168:169], v[168:169], s[6:7] op_sel_hi:[1,0]
	v_perm_b32 v68, v167, v166, s55
	v_perm_b32 v69, v169, v168, s55
	v_lshl_or_b32 v74, v69, 16, v68
	v_pk_mul_f32 v[162:163], v[162:163], s[4:5] op_sel_hi:[1,0]
	v_pk_mul_f32 v[164:165], v[164:165], s[4:5] op_sel_hi:[1,0]
	v_exp_f32_e32 v162, v162
	v_exp_f32_e32 v163, v163
	v_exp_f32_e32 v164, v164
	v_exp_f32_e32 v165, v165
	v_fma_f32 v162, v162, s54, s54 clamp
	v_fma_f32 v163, v163, s54, s54 clamp
	v_fma_f32 v164, v164, s54, s54 clamp
	v_fma_f32 v165, v165, s54, s54 clamp
	v_rcp_f32_e32 v162, v162
	v_rcp_f32_e32 v163, v163
	v_rcp_f32_e32 v164, v164
	v_rcp_f32_e32 v165, v165
	v_pk_add_f32 v[162:163], v[162:163], s[6:7] op_sel_hi:[1,0]
	v_pk_add_f32 v[164:165], v[164:165], s[6:7] op_sel_hi:[1,0]
	v_perm_b32 v68, v163, v162, s55
	v_perm_b32 v69, v165, v164, s55
	v_lshl_or_b32 v75, v69, 16, v68
	v_pk_mul_f32 v[134:135], v[134:135], s[4:5] op_sel_hi:[1,0]
	v_pk_mul_f32 v[136:137], v[136:137], s[4:5] op_sel_hi:[1,0]
	v_exp_f32_e32 v134, v134
	v_exp_f32_e32 v135, v135
	v_exp_f32_e32 v136, v136
	v_exp_f32_e32 v137, v137
	v_fma_f32 v134, v134, s54, s54 clamp
	v_fma_f32 v135, v135, s54, s54 clamp
	v_fma_f32 v136, v136, s54, s54 clamp
	v_fma_f32 v137, v137, s54, s54 clamp
	v_rcp_f32_e32 v134, v134
	v_rcp_f32_e32 v135, v135
	v_rcp_f32_e32 v136, v136
	v_rcp_f32_e32 v137, v137
	v_pk_add_f32 v[134:135], v[134:135], s[6:7] op_sel_hi:[1,0]
	v_pk_add_f32 v[136:137], v[136:137], s[6:7] op_sel_hi:[1,0]
	v_perm_b32 v68, v135, v134, s55
	v_perm_b32 v69, v137, v136, s55
	v_lshl_or_b32 v76, v69, 16, v68
	v_pk_mul_f32 v[130:131], v[130:131], s[4:5] op_sel_hi:[1,0]
	v_pk_mul_f32 v[132:133], v[132:133], s[4:5] op_sel_hi:[1,0]
	v_exp_f32_e32 v130, v130
	v_exp_f32_e32 v131, v131
	v_exp_f32_e32 v132, v132
	v_exp_f32_e32 v133, v133
	v_fma_f32 v130, v130, s54, s54 clamp
	v_fma_f32 v131, v131, s54, s54 clamp
	v_fma_f32 v132, v132, s54, s54 clamp
	v_fma_f32 v133, v133, s54, s54 clamp
	v_rcp_f32_e32 v130, v130
	v_rcp_f32_e32 v131, v131
	v_rcp_f32_e32 v132, v132
	v_rcp_f32_e32 v133, v133
	v_pk_add_f32 v[130:131], v[130:131], s[6:7] op_sel_hi:[1,0]
	v_pk_add_f32 v[132:133], v[132:133], s[6:7] op_sel_hi:[1,0]
	v_perm_b32 v68, v131, v130, s55
	v_perm_b32 v69, v133, v132, s55
	v_lshl_or_b32 v77, v69, 16, v68
	global_store_dwordx4 v[82:83], v[74:77], off
	v_add_u32_e32 v78, 0x80, v18
	v_pk_mul_f32 v[126:127], v[126:127], s[4:5] op_sel_hi:[1,0]
	v_pk_mul_f32 v[60:61], v[60:61], s[4:5] op_sel_hi:[1,0]
	v_exp_f32_e32 v126, v126
	v_exp_f32_e32 v127, v127
	v_exp_f32_e32 v60, v60
	v_exp_f32_e32 v61, v61
	v_fma_f32 v126, v126, s54, s54 clamp
	v_fma_f32 v127, v127, s54, s54 clamp
	v_fma_f32 v60, v60, s54, s54 clamp
	v_fma_f32 v61, v61, s54, s54 clamp
	v_rcp_f32_e32 v126, v126
	v_rcp_f32_e32 v127, v127
	v_rcp_f32_e32 v60, v60
	v_rcp_f32_e32 v61, v61
	v_mad_i64_i32 v[80:81], vcc, v78, s64, v[66:67]
	v_pk_add_f32 v[126:127], v[126:127], s[6:7] op_sel_hi:[1,0]
	v_pk_add_f32 v[60:61], v[60:61], s[6:7] op_sel_hi:[1,0]
	v_perm_b32 v68, v127, v126, s55
	v_perm_b32 v69, v61, v60, s55
	v_lshl_or_b32 v70, v69, 16, v68
	v_pk_mul_f32 v[64:65], v[64:65], s[4:5] op_sel_hi:[1,0]
	v_pk_mul_f32 v[56:57], v[56:57], s[4:5] op_sel_hi:[1,0]
	v_exp_f32_e32 v64, v64
	v_exp_f32_e32 v65, v65
	v_exp_f32_e32 v56, v56
	v_exp_f32_e32 v57, v57
	v_fma_f32 v64, v64, s54, s54 clamp
	v_fma_f32 v65, v65, s54, s54 clamp
	v_fma_f32 v56, v56, s54, s54 clamp
	v_fma_f32 v57, v57, s54, s54 clamp
	v_rcp_f32_e32 v64, v64
	v_rcp_f32_e32 v65, v65
	v_rcp_f32_e32 v56, v56
	v_rcp_f32_e32 v57, v57
	v_pk_add_f32 v[64:65], v[64:65], s[6:7] op_sel_hi:[1,0]
	v_pk_add_f32 v[56:57], v[56:57], s[6:7] op_sel_hi:[1,0]
	v_perm_b32 v68, v65, v64, s55
	v_perm_b32 v69, v57, v56, s55
	v_lshl_or_b32 v71, v69, 16, v68
	v_pk_mul_f32 v[62:63], v[62:63], s[4:5] op_sel_hi:[1,0]
	v_pk_mul_f32 v[54:55], v[54:55], s[4:5] op_sel_hi:[1,0]
	v_exp_f32_e32 v62, v62
	v_exp_f32_e32 v63, v63
	v_exp_f32_e32 v54, v54
	v_exp_f32_e32 v55, v55
	v_fma_f32 v62, v62, s54, s54 clamp
	v_fma_f32 v63, v63, s54, s54 clamp
	v_fma_f32 v54, v54, s54, s54 clamp
	v_fma_f32 v55, v55, s54, s54 clamp
	v_rcp_f32_e32 v62, v62
	v_rcp_f32_e32 v63, v63
	v_rcp_f32_e32 v54, v54
	v_rcp_f32_e32 v55, v55
	v_pk_add_f32 v[62:63], v[62:63], s[6:7] op_sel_hi:[1,0]
	v_pk_add_f32 v[54:55], v[54:55], s[6:7] op_sel_hi:[1,0]
	v_perm_b32 v68, v63, v62, s55
	v_perm_b32 v69, v55, v54, s55
	v_lshl_or_b32 v72, v69, 16, v68
	v_pk_mul_f32 v[58:59], v[58:59], s[4:5] op_sel_hi:[1,0]
	v_pk_mul_f32 v[52:53], v[52:53], s[4:5] op_sel_hi:[1,0]
	v_exp_f32_e32 v58, v58
	v_exp_f32_e32 v59, v59
	v_exp_f32_e32 v52, v52
	v_exp_f32_e32 v53, v53
	v_fma_f32 v58, v58, s54, s54 clamp
	v_fma_f32 v59, v59, s54, s54 clamp
	v_fma_f32 v52, v52, s54, s54 clamp
	v_fma_f32 v53, v53, s54, s54 clamp
	v_rcp_f32_e32 v58, v58
	v_rcp_f32_e32 v59, v59
	v_rcp_f32_e32 v52, v52
	v_rcp_f32_e32 v53, v53
	v_pk_add_f32 v[58:59], v[58:59], s[6:7] op_sel_hi:[1,0]
	v_pk_add_f32 v[52:53], v[52:53], s[6:7] op_sel_hi:[1,0]
	v_perm_b32 v68, v59, v58, s55
	v_perm_b32 v69, v53, v52, s55
	v_lshl_or_b32 v73, v69, 16, v68
	global_store_dwordx4 v[80:81], v[70:73], off
	v_add_u32_e32 v78, 0x90, v18
	v_pk_mul_f32 v[50:51], v[50:51], s[4:5] op_sel_hi:[1,0]
	v_pk_mul_f32 v[44:45], v[44:45], s[4:5] op_sel_hi:[1,0]
	v_exp_f32_e32 v50, v50
	v_exp_f32_e32 v51, v51
	v_exp_f32_e32 v44, v44
	v_exp_f32_e32 v45, v45
	v_fma_f32 v50, v50, s54, s54 clamp
	v_fma_f32 v51, v51, s54, s54 clamp
	v_fma_f32 v44, v44, s54, s54 clamp
	v_fma_f32 v45, v45, s54, s54 clamp
	v_rcp_f32_e32 v50, v50
	v_rcp_f32_e32 v51, v51
	v_rcp_f32_e32 v44, v44
	v_rcp_f32_e32 v45, v45
	v_mad_i64_i32 v[82:83], vcc, v78, s64, v[66:67]
	v_pk_add_f32 v[50:51], v[50:51], s[6:7] op_sel_hi:[1,0]
	v_pk_add_f32 v[44:45], v[44:45], s[6:7] op_sel_hi:[1,0]
	v_perm_b32 v68, v51, v50, s55
	v_perm_b32 v69, v45, v44, s55
	v_lshl_or_b32 v74, v69, 16, v68
	v_pk_mul_f32 v[48:49], v[48:49], s[4:5] op_sel_hi:[1,0]
	v_pk_mul_f32 v[40:41], v[40:41], s[4:5] op_sel_hi:[1,0]
	v_exp_f32_e32 v48, v48
	v_exp_f32_e32 v49, v49
	v_exp_f32_e32 v40, v40
	v_exp_f32_e32 v41, v41
	v_fma_f32 v48, v48, s54, s54 clamp
	v_fma_f32 v49, v49, s54, s54 clamp
	v_fma_f32 v40, v40, s54, s54 clamp
	v_fma_f32 v41, v41, s54, s54 clamp
	v_rcp_f32_e32 v48, v48
	v_rcp_f32_e32 v49, v49
	v_rcp_f32_e32 v40, v40
	v_rcp_f32_e32 v41, v41
	v_pk_add_f32 v[48:49], v[48:49], s[6:7] op_sel_hi:[1,0]
	v_pk_add_f32 v[40:41], v[40:41], s[6:7] op_sel_hi:[1,0]
	v_perm_b32 v68, v49, v48, s55
	v_perm_b32 v69, v41, v40, s55
	v_lshl_or_b32 v75, v69, 16, v68
	v_pk_mul_f32 v[46:47], v[46:47], s[4:5] op_sel_hi:[1,0]
	v_pk_mul_f32 v[38:39], v[38:39], s[4:5] op_sel_hi:[1,0]
	v_exp_f32_e32 v46, v46
	v_exp_f32_e32 v47, v47
	v_exp_f32_e32 v38, v38
	v_exp_f32_e32 v39, v39
	v_fma_f32 v46, v46, s54, s54 clamp
	v_fma_f32 v47, v47, s54, s54 clamp
	v_fma_f32 v38, v38, s54, s54 clamp
	v_fma_f32 v39, v39, s54, s54 clamp
	v_rcp_f32_e32 v46, v46
	v_rcp_f32_e32 v47, v47
	v_rcp_f32_e32 v38, v38
	v_rcp_f32_e32 v39, v39
	v_pk_add_f32 v[46:47], v[46:47], s[6:7] op_sel_hi:[1,0]
	v_pk_add_f32 v[38:39], v[38:39], s[6:7] op_sel_hi:[1,0]
	v_perm_b32 v68, v47, v46, s55
	v_perm_b32 v69, v39, v38, s55
	v_lshl_or_b32 v76, v69, 16, v68
	v_pk_mul_f32 v[42:43], v[42:43], s[4:5] op_sel_hi:[1,0]
	v_pk_mul_f32 v[36:37], v[36:37], s[4:5] op_sel_hi:[1,0]
	v_exp_f32_e32 v42, v42
	v_exp_f32_e32 v43, v43
	v_exp_f32_e32 v36, v36
	v_exp_f32_e32 v37, v37
	v_fma_f32 v42, v42, s54, s54 clamp
	v_fma_f32 v43, v43, s54, s54 clamp
	v_fma_f32 v36, v36, s54, s54 clamp
	v_fma_f32 v37, v37, s54, s54 clamp
	v_rcp_f32_e32 v42, v42
	v_rcp_f32_e32 v43, v43
	v_rcp_f32_e32 v36, v36
	v_rcp_f32_e32 v37, v37
	v_pk_add_f32 v[42:43], v[42:43], s[6:7] op_sel_hi:[1,0]
	v_pk_add_f32 v[36:37], v[36:37], s[6:7] op_sel_hi:[1,0]
	v_perm_b32 v68, v43, v42, s55
	v_perm_b32 v69, v37, v36, s55
	v_lshl_or_b32 v77, v69, 16, v68
	global_store_dwordx4 v[82:83], v[74:77], off
	v_add_u32_e32 v78, 0xa0, v18
	v_pk_mul_f32 v[34:35], v[34:35], s[4:5] op_sel_hi:[1,0]
	v_pk_mul_f32 v[28:29], v[28:29], s[4:5] op_sel_hi:[1,0]
	v_exp_f32_e32 v34, v34
	v_exp_f32_e32 v35, v35
	v_exp_f32_e32 v28, v28
	v_exp_f32_e32 v29, v29
	v_fma_f32 v34, v34, s54, s54 clamp
	v_fma_f32 v35, v35, s54, s54 clamp
	v_fma_f32 v28, v28, s54, s54 clamp
	v_fma_f32 v29, v29, s54, s54 clamp
	v_rcp_f32_e32 v34, v34
	v_rcp_f32_e32 v35, v35
	v_rcp_f32_e32 v28, v28
	v_rcp_f32_e32 v29, v29
	v_mad_i64_i32 v[80:81], vcc, v78, s64, v[66:67]
	v_pk_add_f32 v[34:35], v[34:35], s[6:7] op_sel_hi:[1,0]
	v_pk_add_f32 v[28:29], v[28:29], s[6:7] op_sel_hi:[1,0]
	v_perm_b32 v68, v35, v34, s55
	v_perm_b32 v69, v29, v28, s55
	v_lshl_or_b32 v70, v69, 16, v68
	v_pk_mul_f32 v[32:33], v[32:33], s[4:5] op_sel_hi:[1,0]
	v_pk_mul_f32 v[24:25], v[24:25], s[4:5] op_sel_hi:[1,0]
	v_exp_f32_e32 v32, v32
	v_exp_f32_e32 v33, v33
	v_exp_f32_e32 v24, v24
	v_exp_f32_e32 v25, v25
	v_fma_f32 v32, v32, s54, s54 clamp
	v_fma_f32 v33, v33, s54, s54 clamp
	v_fma_f32 v24, v24, s54, s54 clamp
	v_fma_f32 v25, v25, s54, s54 clamp
	v_rcp_f32_e32 v32, v32
	v_rcp_f32_e32 v33, v33
	v_rcp_f32_e32 v24, v24
	v_rcp_f32_e32 v25, v25
	v_pk_add_f32 v[32:33], v[32:33], s[6:7] op_sel_hi:[1,0]
	v_pk_add_f32 v[24:25], v[24:25], s[6:7] op_sel_hi:[1,0]
	v_perm_b32 v68, v33, v32, s55
	v_perm_b32 v69, v25, v24, s55
	v_lshl_or_b32 v71, v69, 16, v68
	v_pk_mul_f32 v[30:31], v[30:31], s[4:5] op_sel_hi:[1,0]
	v_pk_mul_f32 v[22:23], v[22:23], s[4:5] op_sel_hi:[1,0]
	v_exp_f32_e32 v30, v30
	v_exp_f32_e32 v31, v31
	v_exp_f32_e32 v22, v22
	v_exp_f32_e32 v23, v23
	v_fma_f32 v30, v30, s54, s54 clamp
	v_fma_f32 v31, v31, s54, s54 clamp
	v_fma_f32 v22, v22, s54, s54 clamp
	v_fma_f32 v23, v23, s54, s54 clamp
	v_rcp_f32_e32 v30, v30
	v_rcp_f32_e32 v31, v31
	v_rcp_f32_e32 v22, v22
	v_rcp_f32_e32 v23, v23
	v_pk_add_f32 v[30:31], v[30:31], s[6:7] op_sel_hi:[1,0]
	v_pk_add_f32 v[22:23], v[22:23], s[6:7] op_sel_hi:[1,0]
	v_perm_b32 v68, v31, v30, s55
	v_perm_b32 v69, v23, v22, s55
	v_lshl_or_b32 v72, v69, 16, v68
	v_pk_mul_f32 v[26:27], v[26:27], s[4:5] op_sel_hi:[1,0]
	v_pk_mul_f32 v[20:21], v[20:21], s[4:5] op_sel_hi:[1,0]
	v_exp_f32_e32 v26, v26
	v_exp_f32_e32 v27, v27
	v_exp_f32_e32 v20, v20
	v_exp_f32_e32 v21, v21
	v_fma_f32 v26, v26, s54, s54 clamp
	v_fma_f32 v27, v27, s54, s54 clamp
	v_fma_f32 v20, v20, s54, s54 clamp
	v_fma_f32 v21, v21, s54, s54 clamp
	v_rcp_f32_e32 v26, v26
	v_rcp_f32_e32 v27, v27
	v_rcp_f32_e32 v20, v20
	v_rcp_f32_e32 v21, v21
	v_pk_add_f32 v[26:27], v[26:27], s[6:7] op_sel_hi:[1,0]
	v_pk_add_f32 v[20:21], v[20:21], s[6:7] op_sel_hi:[1,0]
	v_perm_b32 v68, v27, v26, s55
	v_perm_b32 v69, v21, v20, s55
	v_lshl_or_b32 v73, v69, 16, v68
	global_store_dwordx4 v[80:81], v[70:73], off
	v_add_u32_e32 v78, 0xb0, v18
	v_pk_mul_f32 v[16:17], v[16:17], s[4:5] op_sel_hi:[1,0]
	v_pk_mul_f32 v[10:11], v[10:11], s[4:5] op_sel_hi:[1,0]
	v_exp_f32_e32 v16, v16
	v_exp_f32_e32 v17, v17
	v_exp_f32_e32 v10, v10
	v_exp_f32_e32 v11, v11
	v_fma_f32 v16, v16, s54, s54 clamp
	v_fma_f32 v17, v17, s54, s54 clamp
	v_fma_f32 v10, v10, s54, s54 clamp
	v_fma_f32 v11, v11, s54, s54 clamp
	v_rcp_f32_e32 v16, v16
	v_rcp_f32_e32 v17, v17
	v_rcp_f32_e32 v10, v10
	v_rcp_f32_e32 v11, v11
	v_mad_i64_i32 v[82:83], vcc, v78, s64, v[66:67]
	v_pk_add_f32 v[16:17], v[16:17], s[6:7] op_sel_hi:[1,0]
	v_pk_add_f32 v[10:11], v[10:11], s[6:7] op_sel_hi:[1,0]
	v_perm_b32 v68, v17, v16, s55
	v_perm_b32 v69, v11, v10, s55
	v_lshl_or_b32 v74, v69, 16, v68
	v_pk_mul_f32 v[14:15], v[14:15], s[4:5] op_sel_hi:[1,0]
	v_pk_mul_f32 v[6:7], v[6:7], s[4:5] op_sel_hi:[1,0]
	v_exp_f32_e32 v14, v14
	v_exp_f32_e32 v15, v15
	v_exp_f32_e32 v6, v6
	v_exp_f32_e32 v7, v7
	v_fma_f32 v14, v14, s54, s54 clamp
	v_fma_f32 v15, v15, s54, s54 clamp
	v_fma_f32 v6, v6, s54, s54 clamp
	v_fma_f32 v7, v7, s54, s54 clamp
	v_rcp_f32_e32 v14, v14
	v_rcp_f32_e32 v15, v15
	v_rcp_f32_e32 v6, v6
	v_rcp_f32_e32 v7, v7
	v_pk_add_f32 v[14:15], v[14:15], s[6:7] op_sel_hi:[1,0]
	v_pk_add_f32 v[6:7], v[6:7], s[6:7] op_sel_hi:[1,0]
	v_perm_b32 v68, v15, v14, s55
	v_perm_b32 v69, v7, v6, s55
	v_lshl_or_b32 v75, v69, 16, v68
	v_pk_mul_f32 v[12:13], v[12:13], s[4:5] op_sel_hi:[1,0]
	v_pk_mul_f32 v[4:5], v[4:5], s[4:5] op_sel_hi:[1,0]
	v_exp_f32_e32 v12, v12
	v_exp_f32_e32 v13, v13
	v_exp_f32_e32 v4, v4
	v_exp_f32_e32 v5, v5
	v_fma_f32 v12, v12, s54, s54 clamp
	v_fma_f32 v13, v13, s54, s54 clamp
	v_fma_f32 v4, v4, s54, s54 clamp
	v_fma_f32 v5, v5, s54, s54 clamp
	v_rcp_f32_e32 v12, v12
	v_rcp_f32_e32 v13, v13
	v_rcp_f32_e32 v4, v4
	v_rcp_f32_e32 v5, v5
	v_pk_add_f32 v[12:13], v[12:13], s[6:7] op_sel_hi:[1,0]
	v_pk_add_f32 v[4:5], v[4:5], s[6:7] op_sel_hi:[1,0]
	v_perm_b32 v68, v13, v12, s55
	v_perm_b32 v69, v5, v4, s55
	v_lshl_or_b32 v76, v69, 16, v68
	v_pk_mul_f32 v[8:9], v[8:9], s[4:5] op_sel_hi:[1,0]
	v_pk_mul_f32 v[2:3], v[2:3], s[4:5] op_sel_hi:[1,0]
	v_exp_f32_e32 v8, v8
	v_exp_f32_e32 v9, v9
	v_exp_f32_e32 v2, v2
	v_exp_f32_e32 v3, v3
	v_fma_f32 v8, v8, s54, s54 clamp
	v_fma_f32 v9, v9, s54, s54 clamp
	v_fma_f32 v2, v2, s54, s54 clamp
	v_fma_f32 v3, v3, s54, s54 clamp
	v_rcp_f32_e32 v8, v8
	v_rcp_f32_e32 v9, v9
	v_rcp_f32_e32 v2, v2
	v_rcp_f32_e32 v3, v3
	v_pk_add_f32 v[8:9], v[8:9], s[6:7] op_sel_hi:[1,0]
	v_pk_add_f32 v[2:3], v[2:3], s[6:7] op_sel_hi:[1,0]
	v_perm_b32 v68, v9, v8, s55
	v_perm_b32 v69, v3, v2, s55
	v_lshl_or_b32 v77, v69, 16, v68
	global_store_dwordx4 v[82:83], v[74:77], off
	s_andn2_b64 vcc, exec, s[2:3]
	s_mov_b64 s[2:3], -1
	s_cbranch_vccnz .LBB0_3430
	s_branch .LBB0_3536
